# v103 plus the P3 K-loop LDS-DMA pieces in scalar-base form (all four GEMM K-loops uniform)
# speedup vs baseline: 1.0029x; 1.0001x over previous
.LBB0_385:
	ds_read_b128 v[184:187], v174
	ds_read_b128 v[188:191], v175
	ds_read_b128 v[192:195], v174 offset:2048
	ds_read_b128 v[196:199], v175 offset:2048
	ds_read_b128 v[200:203], v174 offset:16384
	ds_read_b128 v[204:207], v175 offset:16384
	ds_read_b128 v[208:211], v174 offset:18432
	ds_read_b128 v[212:215], v175 offset:18432
	s_add_u32 s78, s16, s28
	s_addc_u32 s79, s17, s29
	s_add_i32 m0, s39, 0x8000
	ds_read_b128 v[216:219], v177
	ds_read_b128 v[220:223], v177 offset:2048
	ds_read_b128 v[224:227], v178
	ds_read_b128 v[228:231], v178 offset:2048
	ds_read_b128 v[232:235], v177 offset:4096
	ds_read_b128 v[236:239], v177 offset:6144
	ds_read_b128 v[240:243], v178 offset:4096
	ds_read_b128 v[244:247], v178 offset:6144
	global_load_lds_dwordx4 v150, s[78:79]
	s_add_i32 m0, s39, 0xa000
	s_nop 0
	global_load_lds_dwordx4 v130, s[78:79]
	s_add_i32 m0, s39, 0xc000
	s_nop 0
	global_load_lds_dwordx4 v132, s[78:79]
	s_add_i32 m0, s39, 0xe000
	s_nop 0
	global_load_lds_dwordx4 v134, s[78:79]
	s_waitcnt vmcnt(8)
	s_waitcnt lgkmcnt(0)
	s_barrier
	s_setprio 1
	s_waitcnt lgkmcnt(0)
	v_mfma_f32_16x16x32_bf16 v[126:129], v[184:187], v[216:219], v[126:129]
	s_add_u32 s34, s2, s28
	s_addc_u32 s35, s3, s29
	s_add_u32 s77, s34, 0x63000100
	s_addc_u32 s78, s35, 0
	v_mfma_f32_16x16x32_bf16 v[122:125], v[192:195], v[216:219], v[122:125]
	s_and_b64 s[34:35], s[30:31], exec
	s_cselect_b32 s35, s7, s78
	s_cselect_b32 s34, s6, s77
	s_add_u32 s77, s25, s28
	v_mfma_f32_16x16x32_bf16 v[118:121], v[184:187], v[220:223], v[118:121]
	s_addc_u32 s78, s75, s29
	s_and_b64 s[30:31], s[30:31], exec
	s_cselect_b32 s31, s27, s78
	s_cselect_b32 s30, s26, s77
	v_mfma_f32_16x16x32_bf16 v[114:117], v[192:195], v[220:223], v[114:117]
	v_mfma_f32_16x16x32_bf16 v[110:113], v[184:187], v[232:235], v[110:113]
	v_mfma_f32_16x16x32_bf16 v[102:105], v[192:195], v[232:235], v[102:105]
	v_mfma_f32_16x16x32_bf16 v[94:97], v[184:187], v[236:239], v[94:97]
	v_mfma_f32_16x16x32_bf16 v[86:89], v[192:195], v[236:239], v[86:89]
	v_mfma_f32_16x16x32_bf16 v[126:129], v[188:191], v[224:227], v[126:129]
	v_mfma_f32_16x16x32_bf16 v[122:125], v[196:199], v[224:227], v[122:125]
	v_mfma_f32_16x16x32_bf16 v[118:121], v[188:191], v[228:231], v[118:121]
	v_mfma_f32_16x16x32_bf16 v[114:117], v[196:199], v[228:231], v[114:117]
	v_mfma_f32_16x16x32_bf16 v[110:113], v[188:191], v[240:243], v[110:113]
	v_mfma_f32_16x16x32_bf16 v[102:105], v[196:199], v[240:243], v[102:105]
	v_mfma_f32_16x16x32_bf16 v[94:97], v[188:191], v[244:247], v[94:97]
	v_mfma_f32_16x16x32_bf16 v[86:89], v[196:199], v[244:247], v[86:89]
	s_setprio 0
	s_setprio 1
	v_mfma_f32_16x16x32_bf16 v[106:109], v[200:203], v[216:219], v[106:109]
	v_mfma_f32_16x16x32_bf16 v[98:101], v[208:211], v[216:219], v[98:101]
	v_mfma_f32_16x16x32_bf16 v[90:93], v[200:203], v[220:223], v[90:93]
	v_mfma_f32_16x16x32_bf16 v[82:85], v[208:211], v[220:223], v[82:85]
	v_mfma_f32_16x16x32_bf16 v[78:81], v[200:203], v[232:235], v[78:81]
	v_mfma_f32_16x16x32_bf16 v[74:77], v[208:211], v[232:235], v[74:77]
	v_mfma_f32_16x16x32_bf16 v[70:73], v[200:203], v[236:239], v[70:73]
	v_mfma_f32_16x16x32_bf16 v[66:69], v[208:211], v[236:239], v[66:69]
	v_mfma_f32_16x16x32_bf16 v[106:109], v[204:207], v[224:227], v[106:109]
	v_mfma_f32_16x16x32_bf16 v[98:101], v[212:215], v[224:227], v[98:101]
	v_mfma_f32_16x16x32_bf16 v[90:93], v[204:207], v[228:231], v[90:93]
	v_mfma_f32_16x16x32_bf16 v[82:85], v[212:215], v[228:231], v[82:85]
	v_mfma_f32_16x16x32_bf16 v[78:81], v[204:207], v[240:243], v[78:81]
	v_mfma_f32_16x16x32_bf16 v[74:77], v[212:215], v[240:243], v[74:77]
	v_mfma_f32_16x16x32_bf16 v[70:73], v[204:207], v[244:247], v[70:73]
	v_mfma_f32_16x16x32_bf16 v[66:69], v[212:215], v[244:247], v[66:69]
	s_setprio 0
	s_barrier
	s_add_i32 s77, s45, s33
	s_mov_b32 m0, s77
	ds_read_b128 v[216:219], v177 offset:16384
	ds_read_b128 v[220:223], v177 offset:18432
	ds_read_b128 v[224:227], v178 offset:16384
	ds_read_b128 v[228:231], v178 offset:18432
	ds_read_b128 v[232:235], v177 offset:20480
	ds_read_b128 v[236:239], v177 offset:22528
	ds_read_b128 v[240:243], v178 offset:20480
	ds_read_b128 v[244:247], v178 offset:22528
	global_load_lds_dwordx4 v146, s[30:31]
	s_add_i32 m0, s77, 0x2000
	s_add_u32 s78, s30, 0x80000
	s_addc_u32 s79, s31, 0
	s_add_i32 s77, s47, s33
	global_load_lds_dwordx4 v148, s[30:31]
	s_mov_b32 m0, s77
	s_nop 0
	global_load_lds_dwordx4 v146, s[78:79]
	s_add_i32 m0, s77, 0x2000
	s_nop 0
	global_load_lds_dwordx4 v148, s[78:79]
	s_waitcnt vmcnt(6)
	s_waitcnt lgkmcnt(0)
	s_barrier
	s_setprio 1
	s_waitcnt lgkmcnt(0)
	v_mfma_f32_16x16x32_bf16 v[62:65], v[184:187], v[216:219], v[62:65]
	v_mfma_f32_16x16x32_bf16 v[58:61], v[192:195], v[216:219], v[58:61]
	v_mfma_f32_16x16x32_bf16 v[50:53], v[184:187], v[220:223], v[50:53]
	v_mfma_f32_16x16x32_bf16 v[42:45], v[192:195], v[220:223], v[42:45]
	v_mfma_f32_16x16x32_bf16 v[34:37], v[184:187], v[232:235], v[34:37]
	v_mfma_f32_16x16x32_bf16 v[26:29], v[192:195], v[232:235], v[26:29]
	v_mfma_f32_16x16x32_bf16 v[18:21], v[184:187], v[236:239], v[18:21]
	v_mfma_f32_16x16x32_bf16 v[10:13], v[192:195], v[236:239], v[10:13]
	v_mfma_f32_16x16x32_bf16 v[62:65], v[188:191], v[224:227], v[62:65]
	v_mfma_f32_16x16x32_bf16 v[58:61], v[196:199], v[224:227], v[58:61]
	v_mfma_f32_16x16x32_bf16 v[50:53], v[188:191], v[228:231], v[50:53]
	v_mfma_f32_16x16x32_bf16 v[42:45], v[196:199], v[228:231], v[42:45]
	v_mfma_f32_16x16x32_bf16 v[34:37], v[188:191], v[240:243], v[34:37]
	v_mfma_f32_16x16x32_bf16 v[26:29], v[196:199], v[240:243], v[26:29]
	v_mfma_f32_16x16x32_bf16 v[18:21], v[188:191], v[244:247], v[18:21]
	v_mfma_f32_16x16x32_bf16 v[10:13], v[196:199], v[244:247], v[10:13]
	s_setprio 0
	s_setprio 1
	v_mfma_f32_16x16x32_bf16 v[54:57], v[200:203], v[216:219], v[54:57]
	v_mfma_f32_16x16x32_bf16 v[46:49], v[208:211], v[216:219], v[46:49]
	v_mfma_f32_16x16x32_bf16 v[38:41], v[200:203], v[220:223], v[38:41]
	v_mfma_f32_16x16x32_bf16 v[30:33], v[208:211], v[220:223], v[30:33]
	v_mfma_f32_16x16x32_bf16 v[22:25], v[200:203], v[232:235], v[22:25]
	v_mfma_f32_16x16x32_bf16 v[14:17], v[208:211], v[232:235], v[14:17]
	v_mfma_f32_16x16x32_bf16 v[6:9], v[200:203], v[236:239], v[6:9]
	v_mfma_f32_16x16x32_bf16 v[2:5], v[208:211], v[236:239], v[2:5]
	v_mfma_f32_16x16x32_bf16 v[54:57], v[204:207], v[224:227], v[54:57]
	v_mfma_f32_16x16x32_bf16 v[46:49], v[212:215], v[224:227], v[46:49]
	v_mfma_f32_16x16x32_bf16 v[38:41], v[204:207], v[228:231], v[38:41]
	v_mfma_f32_16x16x32_bf16 v[30:33], v[212:215], v[228:231], v[30:33]
	v_mfma_f32_16x16x32_bf16 v[22:25], v[204:207], v[240:243], v[22:25]
	v_mfma_f32_16x16x32_bf16 v[14:17], v[212:215], v[240:243], v[14:17]
	v_mfma_f32_16x16x32_bf16 v[6:9], v[204:207], v[244:247], v[6:9]
	v_mfma_f32_16x16x32_bf16 v[2:5], v[212:215], v[244:247], v[2:5]
	s_setprio 0
	s_barrier
